# grid barrier: all waiters poll the global arrival counter (last XCD leader's arrival is the release; generation words no longer bumped) + fused conversion/stagger, on top of v017
# speedup vs baseline: 1.0022x; 1.0022x over previous
.LBB0_180:
	s_or_b64 exec, exec, s[4:5]
	v_cvt_f32_u32_e32 v6, v3
	s_waitcnt vmcnt(0)
	v_readfirstlane_b32 s4, v5
	v_sub_u32_e32 v5, 0, v3
	v_rcp_iflag_f32_e32 v6, v6
	v_add_u32_e32 v7, s4, v4
	v_mul_f32_e32 v6, 0x4f7ffffe, v6
	v_cvt_u32_f32_e32 v6, v6
	v_mul_lo_u32 v4, v5, v6
	v_mul_hi_u32 v4, v6, v4
	v_add_u32_e32 v4, v6, v4
	v_mul_hi_u32 v4, v7, v4
	v_mul_lo_u32 v5, v4, v3
	v_sub_u32_e32 v5, v7, v5
	v_add_u32_e32 v6, 1, v4
	v_cmp_ge_u32_e32 vcc, v5, v3
	s_nop 1
	v_cndmask_b32_e32 v4, v4, v6, vcc
	v_sub_u32_e32 v6, v5, v3
	v_cndmask_b32_e32 v5, v5, v6, vcc
	v_add_u32_e32 v6, 1, v4
	v_cmp_ge_u32_e32 vcc, v5, v3
	v_add_u32_e32 v5, 1, v7
	s_nop 0
	v_cndmask_b32_e32 v4, v4, v6, vcc
	v_mul_lo_u32 v6, v3, v4
	v_add_u32_e32 v3, v6, v3
	v_cmp_ne_u32_e32 vcc, v5, v3
	s_and_saveexec_b64 s[4:5], vcc
	s_xor_b64 s[4:5], exec, s[4:5]
	s_cbranch_execz .LBB0_194
	v_mad_u32_u24 v6, v4, v2, v2
	v_readlane_b32 s6, v254, 18
	v_readlane_b32 s7, v254, 19
	s_waitcnt lgkmcnt(0)
	s_nop 3
	global_load_dword v2, v207, s[6:7] sc1
	s_waitcnt vmcnt(0)
	v_cmp_lt_u32_e32 vcc, v2, v6
	s_and_saveexec_b64 s[6:7], vcc
	s_cbranch_execz .LBB0_193
	s_mov_b32 s23, 1
	s_mov_b64 s[8:9], 0
	s_branch .LBB0_184

.LBB0_186:
	v_readlane_b32 s14, v254, 18
	v_readlane_b32 s15, v254, 19
	s_add_i32 s23, s23, 1
	s_mov_b64 s[16:17], -1
	s_nop 2
	global_load_dword v2, v207, s[14:15] sc1
	s_waitcnt vmcnt(0)
	v_cmp_ge_u32_e32 vcc, v2, v6
	s_orn2_b64 s[14:15], vcc, exec
	s_branch .LBB0_183

.LBB0_199:
	s_or_b64 exec, exec, s[4:5]
	v_cvt_f32_u32_e32 v5, v2
	s_waitcnt vmcnt(0)
	v_readfirstlane_b32 s4, v4
	v_sub_u32_e32 v4, 0, v2
	v_rcp_iflag_f32_e32 v5, v5
	v_add_u32_e32 v6, s4, v3
	v_mul_f32_e32 v5, 0x4f7ffffe, v5
	v_cvt_u32_f32_e32 v5, v5
	v_mul_lo_u32 v3, v4, v5
	v_mul_hi_u32 v3, v5, v3
	v_add_u32_e32 v3, v5, v3
	v_mul_hi_u32 v3, v6, v3
	v_mul_lo_u32 v4, v3, v2
	v_sub_u32_e32 v4, v6, v4
	v_add_u32_e32 v5, 1, v3
	v_cmp_ge_u32_e32 vcc, v4, v2
	s_nop 1
	v_cndmask_b32_e32 v3, v3, v5, vcc
	v_sub_u32_e32 v5, v4, v2
	v_cndmask_b32_e32 v4, v4, v5, vcc
	v_add_u32_e32 v5, 1, v3
	v_cmp_ge_u32_e32 vcc, v4, v2
	v_add_u32_e32 v4, 1, v6
	s_nop 0
	v_cndmask_b32_e32 v3, v3, v5, vcc
	v_mul_lo_u32 v5, v2, v3
	v_add_u32_e32 v2, v5, v2
	v_cmp_ne_u32_e32 vcc, v4, v2
	s_and_saveexec_b64 s[4:5], vcc
	s_xor_b64 s[4:5], exec, s[4:5]
	s_cbranch_execz .LBB0_213
	v_mov_b32_e32 v5, v2
	v_readlane_b32 s6, v254, 18
	v_readlane_b32 s7, v254, 19
	s_nop 4
	global_load_dword v2, v207, s[6:7] sc1
	s_waitcnt vmcnt(0)
	v_cmp_lt_u32_e32 vcc, v2, v5
	s_and_saveexec_b64 s[6:7], vcc
	s_cbranch_execz .LBB0_212
	s_mov_b32 s23, 1
	s_mov_b64 s[8:9], 0
	s_branch .LBB0_203

.LBB0_205:
	v_readlane_b32 s14, v254, 18
	v_readlane_b32 s15, v254, 19
	s_add_i32 s23, s23, 1
	s_mov_b64 s[16:17], -1
	s_nop 2
	global_load_dword v2, v207, s[14:15] sc1
	s_waitcnt vmcnt(0)
	v_cmp_ge_u32_e32 vcc, v2, v5
	s_orn2_b64 s[14:15], vcc, exec
	s_branch .LBB0_202

.LBB0_215:
	s_ff1_i32_b64 s9, s[6:7]
	v_readlane_b32 s12, v2, s9
	s_add_i32 s8, s8, s12
	s_lshl_b64 s[12:13], 1, s9
	s_andn2_b64 s[6:7], s[6:7], s[12:13]
	s_cmp_lg_u64 s[6:7], 0
	s_cbranch_scc1 .LBB0_215
	v_mbcnt_lo_u32_b32 v2, exec_lo, 0
	v_mbcnt_hi_u32_b32 v2, exec_hi, v2
	v_cmp_eq_u32_e32 vcc, 0, v2
	s_and_saveexec_b64 s[6:7], vcc
	s_xor_b64 s[6:7], exec, s[6:7]
	s_cbranch_execz .LBB0_218
	v_mov_b32_e32 v2, s8
	v_readlane_b32 s8, v254, 20
	v_readlane_b32 s9, v254, 21
	s_nop 4
.LBB0_218:
	s_or_b64 exec, exec, s[6:7]

.LBB0_296:
	s_or_b64 exec, exec, s[4:5]
	v_cvt_f32_u32_e32 v6, v3
	s_waitcnt vmcnt(0)
	v_readfirstlane_b32 s4, v5
	v_sub_u32_e32 v5, 0, v3
	v_rcp_iflag_f32_e32 v6, v6
	v_add_u32_e32 v7, s4, v4
	v_mul_f32_e32 v6, 0x4f7ffffe, v6
	v_cvt_u32_f32_e32 v6, v6
	v_mul_lo_u32 v4, v5, v6
	v_mul_hi_u32 v4, v6, v4
	v_add_u32_e32 v4, v6, v4
	v_mul_hi_u32 v4, v7, v4
	v_mul_lo_u32 v5, v4, v3
	v_sub_u32_e32 v5, v7, v5
	v_add_u32_e32 v6, 1, v4
	v_cmp_ge_u32_e32 vcc, v5, v3
	s_nop 1
	v_cndmask_b32_e32 v4, v4, v6, vcc
	v_sub_u32_e32 v6, v5, v3
	v_cndmask_b32_e32 v5, v5, v6, vcc
	v_add_u32_e32 v6, 1, v4
	v_cmp_ge_u32_e32 vcc, v5, v3
	v_add_u32_e32 v5, 1, v7
	s_nop 0
	v_cndmask_b32_e32 v4, v4, v6, vcc
	v_mul_lo_u32 v6, v3, v4
	v_add_u32_e32 v3, v6, v3
	v_cmp_ne_u32_e32 vcc, v5, v3
	s_and_saveexec_b64 s[4:5], vcc
	s_xor_b64 s[4:5], exec, s[4:5]
	s_cbranch_execz .LBB0_310
	v_mad_u32_u24 v6, v4, v2, v2
	v_readlane_b32 s6, v254, 18
	v_readlane_b32 s7, v254, 19
	s_waitcnt lgkmcnt(0)
	s_nop 3
	global_load_dword v2, v207, s[6:7] sc1
	s_waitcnt vmcnt(0)
	v_cmp_lt_u32_e32 vcc, v2, v6
	s_and_saveexec_b64 s[6:7], vcc
	s_cbranch_execz .LBB0_309
	s_mov_b32 s10, 1
	s_mov_b64 s[8:9], 0
	s_branch .LBB0_300

.LBB0_302:
	v_readlane_b32 s14, v254, 18
	v_readlane_b32 s15, v254, 19
	s_add_i32 s10, s10, 1
	s_mov_b64 s[16:17], -1
	s_nop 2
	global_load_dword v2, v207, s[14:15] sc1
	s_waitcnt vmcnt(0)
	v_cmp_ge_u32_e32 vcc, v2, v6
	s_orn2_b64 s[14:15], vcc, exec
	s_branch .LBB0_299

.LBB0_315:
	s_or_b64 exec, exec, s[6:7]
	v_cvt_f32_u32_e32 v5, v2
	s_waitcnt vmcnt(0)
	v_readfirstlane_b32 s6, v4
	v_sub_u32_e32 v4, 0, v2
	v_rcp_iflag_f32_e32 v5, v5
	v_add_u32_e32 v6, s6, v3
	v_mul_f32_e32 v5, 0x4f7ffffe, v5
	v_cvt_u32_f32_e32 v5, v5
	v_mul_lo_u32 v3, v4, v5
	v_mul_hi_u32 v3, v5, v3
	v_add_u32_e32 v3, v5, v3
	v_mul_hi_u32 v3, v6, v3
	v_mul_lo_u32 v4, v3, v2
	v_sub_u32_e32 v4, v6, v4
	v_add_u32_e32 v5, 1, v3
	v_cmp_ge_u32_e32 vcc, v4, v2
	s_nop 1
	v_cndmask_b32_e32 v3, v3, v5, vcc
	v_sub_u32_e32 v5, v4, v2
	v_cndmask_b32_e32 v4, v4, v5, vcc
	v_add_u32_e32 v5, 1, v3
	v_cmp_ge_u32_e32 vcc, v4, v2
	v_add_u32_e32 v4, 1, v6
	s_nop 0
	v_cndmask_b32_e32 v3, v3, v5, vcc
	v_mul_lo_u32 v5, v2, v3
	v_add_u32_e32 v2, v5, v2
	v_cmp_ne_u32_e32 vcc, v4, v2
	s_and_saveexec_b64 s[6:7], vcc
	s_xor_b64 s[6:7], exec, s[6:7]
	s_cbranch_execz .LBB0_329
	v_mov_b32_e32 v5, v2
	v_readlane_b32 s8, v254, 18
	v_readlane_b32 s9, v254, 19
	s_nop 4
	global_load_dword v2, v207, s[8:9] sc1
	s_waitcnt vmcnt(0)
	v_cmp_lt_u32_e32 vcc, v2, v5
	s_and_saveexec_b64 s[8:9], vcc
	s_cbranch_execz .LBB0_328
	s_mov_b32 s10, 1
	s_mov_b64 s[12:13], 0
	s_branch .LBB0_319

.LBB0_321:
	v_readlane_b32 s16, v254, 18
	v_readlane_b32 s17, v254, 19
	s_add_i32 s10, s10, 1
	s_mov_b64 s[24:25], -1
	s_nop 2
	global_load_dword v2, v207, s[16:17] sc1
	s_waitcnt vmcnt(0)
	v_cmp_ge_u32_e32 vcc, v2, v5
	s_orn2_b64 s[16:17], vcc, exec
	s_branch .LBB0_318

.LBB0_331:
	s_ff1_i32_b64 s12, s[8:9]
	v_readlane_b32 s13, v2, s12
	s_add_i32 s10, s10, s13
	s_lshl_b64 s[12:13], 1, s12
	s_andn2_b64 s[8:9], s[8:9], s[12:13]
	s_cmp_lg_u64 s[8:9], 0
	s_cbranch_scc1 .LBB0_331
	v_mbcnt_lo_u32_b32 v2, exec_lo, 0
	v_mbcnt_hi_u32_b32 v2, exec_hi, v2
	v_cmp_eq_u32_e32 vcc, 0, v2
	s_and_saveexec_b64 s[8:9], vcc
	s_xor_b64 s[8:9], exec, s[8:9]
	s_cbranch_execz .LBB0_334
	v_readlane_b32 s12, v254, 20
	v_mov_b32_e32 v2, s10
	v_readlane_b32 s13, v254, 21
	s_nop 4
.LBB0_334:
	s_or_b64 exec, exec, s[8:9]

.LBB0_402:
	s_ff1_i32_b64 s9, s[6:7]
	v_readlane_b32 s12, v2, s9
	s_add_i32 s8, s8, s12
	s_lshl_b64 s[12:13], 1, s9
	s_andn2_b64 s[6:7], s[6:7], s[12:13]
	s_cmp_lg_u64 s[6:7], 0
	s_cbranch_scc1 .LBB0_402
	v_mbcnt_lo_u32_b32 v2, exec_lo, 0
	v_mbcnt_hi_u32_b32 v2, exec_hi, v2
	v_cmp_eq_u32_e32 vcc, 0, v2
	s_and_saveexec_b64 s[6:7], vcc
	s_xor_b64 s[6:7], exec, s[6:7]
	s_cbranch_execz .LBB0_405
	v_mov_b32_e32 v2, s8
	v_readlane_b32 s8, v254, 20
	v_readlane_b32 s9, v254, 21
	s_nop 4
.LBB0_405:
	s_or_b64 exec, exec, s[6:7]

.LBB0_541:
	s_or_b64 exec, exec, s[4:5]
	v_cvt_f32_u32_e32 v5, v2
	s_waitcnt vmcnt(0)
	v_readfirstlane_b32 s4, v4
	v_sub_u32_e32 v4, 0, v2
	v_rcp_iflag_f32_e32 v5, v5
	v_add_u32_e32 v6, s4, v3
	v_mul_f32_e32 v5, 0x4f7ffffe, v5
	v_cvt_u32_f32_e32 v5, v5
	v_mul_lo_u32 v3, v4, v5
	v_mul_hi_u32 v3, v5, v3
	v_add_u32_e32 v3, v5, v3
	v_mul_hi_u32 v3, v6, v3
	v_mul_lo_u32 v4, v3, v2
	v_sub_u32_e32 v4, v6, v4
	v_add_u32_e32 v5, 1, v3
	v_cmp_ge_u32_e32 vcc, v4, v2
	s_nop 1
	v_cndmask_b32_e32 v3, v3, v5, vcc
	v_sub_u32_e32 v5, v4, v2
	v_cndmask_b32_e32 v4, v4, v5, vcc
	v_add_u32_e32 v5, 1, v3
	v_cmp_ge_u32_e32 vcc, v4, v2
	v_add_u32_e32 v4, 1, v6
	s_nop 0
	v_cndmask_b32_e32 v3, v3, v5, vcc
	v_mul_lo_u32 v5, v2, v3
	v_add_u32_e32 v2, v5, v2
	v_cmp_ne_u32_e32 vcc, v4, v2
	s_and_saveexec_b64 s[4:5], vcc
	s_xor_b64 s[4:5], exec, s[4:5]
	s_cbranch_execz .LBB0_555
	v_mov_b32_e32 v5, v2
	v_readlane_b32 s6, v254, 18
	v_readlane_b32 s7, v254, 19
	s_nop 4
	global_load_dword v2, v207, s[6:7] sc1
	s_waitcnt vmcnt(0)
	v_cmp_lt_u32_e32 vcc, v2, v5
	s_and_saveexec_b64 s[6:7], vcc
	s_cbranch_execz .LBB0_554
	s_mov_b32 s10, 1
	s_mov_b64 s[8:9], 0
	s_branch .LBB0_545

.LBB0_547:
	v_readlane_b32 s14, v254, 18
	v_readlane_b32 s15, v254, 19
	s_add_i32 s10, s10, 1
	s_mov_b64 s[16:17], -1
	s_nop 2
	global_load_dword v2, v207, s[14:15] sc1
	s_waitcnt vmcnt(0)
	v_cmp_ge_u32_e32 vcc, v2, v5
	s_orn2_b64 s[14:15], vcc, exec
	s_branch .LBB0_544

.LBB0_557:
	s_ff1_i32_b64 s9, s[6:7]
	v_readlane_b32 s10, v2, s9
	s_lshl_b64 s[12:13], 1, s9
	s_add_i32 s8, s8, s10
	s_andn2_b64 s[6:7], s[6:7], s[12:13]
	s_cmp_lg_u64 s[6:7], 0
	s_cbranch_scc1 .LBB0_557
	v_mbcnt_lo_u32_b32 v2, exec_lo, 0
	v_mbcnt_hi_u32_b32 v2, exec_hi, v2
	v_cmp_eq_u32_e32 vcc, 0, v2
	s_and_saveexec_b64 s[6:7], vcc
	s_xor_b64 s[6:7], exec, s[6:7]
	s_cbranch_execz .LBB0_560
	v_mov_b32_e32 v2, s8
	v_readlane_b32 s8, v254, 20
	v_readlane_b32 s9, v254, 21
	s_nop 4
.LBB0_560:
	s_or_b64 exec, exec, s[6:7]

.LBB0_661:
	s_ff1_i32_b64 s9, s[6:7]
	v_readlane_b32 s12, v2, s9
	s_add_i32 s8, s8, s12
	s_lshl_b64 s[12:13], 1, s9
	s_andn2_b64 s[6:7], s[6:7], s[12:13]
	s_cmp_lg_u64 s[6:7], 0
	s_cbranch_scc1 .LBB0_661
	v_mbcnt_lo_u32_b32 v2, exec_lo, 0
	v_mbcnt_hi_u32_b32 v2, exec_hi, v2
	v_cmp_eq_u32_e32 vcc, 0, v2
	s_and_saveexec_b64 s[6:7], vcc
	s_xor_b64 s[6:7], exec, s[6:7]
	s_cbranch_execz .LBB0_664
	v_mov_b32_e32 v2, s8
	v_readlane_b32 s8, v254, 20
	v_readlane_b32 s9, v254, 21
	s_nop 4
.LBB0_664:
	s_or_b64 exec, exec, s[6:7]

.LBB0_746:
	s_ff1_i32_b64 s9, s[6:7]
	v_readlane_b32 s12, v2, s9
	s_add_i32 s8, s8, s12
	s_lshl_b64 s[12:13], 1, s9
	s_andn2_b64 s[6:7], s[6:7], s[12:13]
	s_cmp_lg_u64 s[6:7], 0
	s_cbranch_scc1 .LBB0_746
	v_mbcnt_lo_u32_b32 v2, exec_lo, 0
	v_mbcnt_hi_u32_b32 v2, exec_hi, v2
	v_cmp_eq_u32_e32 vcc, 0, v2
	s_and_saveexec_b64 s[6:7], vcc
	s_xor_b64 s[6:7], exec, s[6:7]
	s_cbranch_execz .LBB0_749
	v_mov_b32_e32 v2, s8
	v_readlane_b32 s8, v254, 20
	v_readlane_b32 s9, v254, 21
	s_nop 4
.LBB0_749:
	s_or_b64 exec, exec, s[6:7]

.LBB0_909:
	s_ff1_i32_b64 s9, s[6:7]
	v_readlane_b32 s10, v2, s9
	s_lshl_b64 s[12:13], 1, s9
	s_add_i32 s8, s8, s10
	s_andn2_b64 s[6:7], s[6:7], s[12:13]
	s_cmp_lg_u64 s[6:7], 0
	s_cbranch_scc1 .LBB0_909
	v_mbcnt_lo_u32_b32 v2, exec_lo, 0
	v_mbcnt_hi_u32_b32 v2, exec_hi, v2
	v_cmp_eq_u32_e32 vcc, 0, v2
	s_and_saveexec_b64 s[6:7], vcc
	s_xor_b64 s[6:7], exec, s[6:7]
	s_cbranch_execz .LBB0_912
	v_mov_b32_e32 v2, s8
	v_readlane_b32 s8, v254, 20
	v_readlane_b32 s9, v254, 21
	s_nop 4
.LBB0_912:
	s_or_b64 exec, exec, s[6:7]

.LBB0_991:
	s_ff1_i32_b64 s9, s[6:7]
	v_readlane_b32 s12, v2, s9
	s_add_i32 s8, s8, s12
	s_lshl_b64 s[12:13], 1, s9
	s_andn2_b64 s[6:7], s[6:7], s[12:13]
	s_cmp_lg_u64 s[6:7], 0
	s_cbranch_scc1 .LBB0_991
	v_mbcnt_lo_u32_b32 v2, exec_lo, 0
	v_mbcnt_hi_u32_b32 v2, exec_hi, v2
	v_cmp_eq_u32_e32 vcc, 0, v2
	s_and_saveexec_b64 s[6:7], vcc
	s_xor_b64 s[6:7], exec, s[6:7]
	s_cbranch_execz .LBB0_994
	v_mov_b32_e32 v2, s8
	v_readlane_b32 s8, v254, 20
	v_readlane_b32 s9, v254, 21
	s_nop 4
.LBB0_994:
	s_or_b64 exec, exec, s[6:7]

.LBB0_1223:
	s_ff1_i32_b64 s9, s[6:7]
	v_readlane_b32 s10, v2, s9
	s_lshl_b64 s[12:13], 1, s9
	s_add_i32 s8, s8, s10
	s_andn2_b64 s[6:7], s[6:7], s[12:13]
	s_cmp_lg_u64 s[6:7], 0
	s_cbranch_scc1 .LBB0_1223
	v_mbcnt_lo_u32_b32 v2, exec_lo, 0
	v_mbcnt_hi_u32_b32 v2, exec_hi, v2
	v_cmp_eq_u32_e32 vcc, 0, v2
	s_and_saveexec_b64 s[6:7], vcc
	s_xor_b64 s[6:7], exec, s[6:7]
	s_cbranch_execz .LBB0_1226
	v_mov_b32_e32 v2, s8
	v_readlane_b32 s8, v254, 20
	v_readlane_b32 s9, v254, 21
	s_nop 4
.LBB0_1226:
	s_or_b64 exec, exec, s[6:7]

.LBB0_1328:
	s_ff1_i32_b64 s9, s[6:7]
	v_readlane_b32 s12, v2, s9
	s_add_i32 s8, s8, s12
	s_lshl_b64 s[12:13], 1, s9
	s_andn2_b64 s[6:7], s[6:7], s[12:13]
	s_cmp_lg_u64 s[6:7], 0
	s_cbranch_scc1 .LBB0_1328
	v_mbcnt_lo_u32_b32 v2, exec_lo, 0
	v_mbcnt_hi_u32_b32 v2, exec_hi, v2
	v_cmp_eq_u32_e32 vcc, 0, v2
	s_and_saveexec_b64 s[6:7], vcc
	s_xor_b64 s[6:7], exec, s[6:7]
	s_cbranch_execz .LBB0_1331
	v_mov_b32_e32 v2, s8
	v_readlane_b32 s8, v254, 20
	v_readlane_b32 s9, v254, 21
	s_nop 4
.LBB0_1331:
	s_or_b64 exec, exec, s[6:7]

.LBB0_1413:
	s_ff1_i32_b64 s9, s[6:7]
	v_readlane_b32 s12, v2, s9
	s_add_i32 s8, s8, s12
	s_lshl_b64 s[12:13], 1, s9
	s_andn2_b64 s[6:7], s[6:7], s[12:13]
	s_cmp_lg_u64 s[6:7], 0
	s_cbranch_scc1 .LBB0_1413
	v_mbcnt_lo_u32_b32 v2, exec_lo, 0
	v_mbcnt_hi_u32_b32 v2, exec_hi, v2
	v_cmp_eq_u32_e32 vcc, 0, v2
	s_and_saveexec_b64 s[6:7], vcc
	s_xor_b64 s[6:7], exec, s[6:7]
	s_cbranch_execz .LBB0_1416
	v_mov_b32_e32 v2, s8
	v_readlane_b32 s8, v254, 20
	v_readlane_b32 s9, v254, 21
	s_nop 4
.LBB0_1416:
	s_or_b64 exec, exec, s[6:7]

.LBB0_1525:
	s_ff1_i32_b64 s9, s[6:7]
	v_readlane_b32 s10, v2, s9
	s_lshl_b64 s[12:13], 1, s9
	s_add_i32 s8, s8, s10
	s_andn2_b64 s[6:7], s[6:7], s[12:13]
	s_cmp_lg_u64 s[6:7], 0
	s_cbranch_scc1 .LBB0_1525
	v_mbcnt_lo_u32_b32 v2, exec_lo, 0
	v_mbcnt_hi_u32_b32 v2, exec_hi, v2
	v_cmp_eq_u32_e32 vcc, 0, v2
	s_and_saveexec_b64 s[6:7], vcc
	s_xor_b64 s[6:7], exec, s[6:7]
	s_cbranch_execz .LBB0_1528
	v_mov_b32_e32 v2, s8
	v_readlane_b32 s8, v254, 20
	v_readlane_b32 s9, v254, 21
	s_nop 4
.LBB0_1528:
	s_or_b64 exec, exec, s[6:7]
